# baseline (speedup 1.0000x reference)
_Z10attn64_fwdPKtS0_S0_Pt8PrepArgs:
	s_mov_b64 s[4:5], -1
	s_cmpk_lt_u32 s2, 0x300
	v_lshlrev_b32_e32 v1, 4, v0
	s_cbranch_scc0 .LBB1_53
	s_lshr_b32 s12, s2, 4
	s_and_b32 s3, s2, 7
	s_and_b32 s12, s12, 56
	s_or_b32 s3, s12, s3
	s_mul_i32 s12, s3, 43
	s_lshr_b32 s14, s12, 9
	s_mul_i32 s12, s14, 12
	v_readfirstlane_b32 s15, v0
	s_lshl_b32 s13, s2, 4
	s_load_dwordx8 s[4:11], s[0:1], 0x0
	s_sub_i32 s3, s3, s12
	s_lshr_b32 s24, s15, 6
	s_bitcmp1_b32 s15, 8
	s_cbranch_scc0 .Lattn_noprio
	s_setprio 1
.Lattn_noprio:
	s_lshl_b32 s12, s14, 11
	s_and_b32 s13, s13, 0x780
	s_or_b32 s12, s12, s13
	s_lshl_b32 s13, s24, 5
	s_add_i32 s12, s12, s13
	s_mul_hi_u32 s13, s12, 0x300
	s_mulk_i32 s12, 0x300
	s_lshl_b64 s[12:13], s[12:13], 1
	s_waitcnt lgkmcnt(0)
	s_add_u32 s4, s4, s12
	s_addc_u32 s5, s5, s13
	s_and_b32 s16, s3, 0xff
	s_lshl_b32 s3, s16, 6
	s_lshl_b32 s17, s16, 7
	s_add_u32 s18, s4, s17
	s_addc_u32 s19, s5, 0
	s_and_b32 s16, s15, 0x3fffffc0
	s_mul_i32 s14, s14, 0x300000
	s_add_u32 s4, s6, s14
	v_and_b32_e32 v212, 63, v0
	s_addc_u32 s5, s7, 0
	s_add_u32 s4, s4, s17
	v_mul_u32_u24_e32 v2, 0x300, v212
	s_addc_u32 s5, s5, 0
	v_lshlrev_b32_e32 v200, 1, v2
	v_mov_b32_e32 v201, 0
	s_lshl_b32 s20, s24, 4
	v_lshl_add_u64 v[2:3], s[4:5], 0, v[200:201]
	s_add_u32 s4, s8, s14
	s_addc_u32 s5, s9, 0
	s_mov_b32 s21, 0
	s_add_u32 s4, s4, s17
	v_lshl_add_u64 v[198:199], v[2:3], 0, s[20:21]
	s_addc_u32 s5, s5, 0
	v_bfe_u32 v2, v0, 2, 4
	s_lshr_b32 s6, s15, 2
	v_and_or_b32 v2, s6, 48, v2
	v_mul_u32_u24_e32 v2, 0x300, v2
	s_and_b32 s20, s6, 0x3fffffc0
	s_lshl_b32 s27, s24, 10
	v_lshlrev_b32_e32 v200, 1, v2
	s_cmp_lg_u32 0, -1
	v_lshl_add_u64 v[2:3], s[4:5], 0, v[200:201]
	v_lshlrev_b32_e32 v213, 3, v0
	s_cselect_b32 s4, 0, 0
	v_and_b32_e32 v50, 24, v213
	s_add_i32 s29, s27, s4
	s_mov_b32 s4, m0
	s_mov_b32 m0, s29
	s_nop 0
	global_load_lds_dwordx4 v[198:199], off
	s_mov_b32 m0, s4
	v_lshl_add_u64 v[2:3], v[2:3], 0, s[20:21]
	v_lshlrev_b32_e32 v200, 1, v50
	v_lshl_add_u64 v[194:195], v[198:199], 0, 64
	s_add_i32 s28, s29, 0x1000
	s_mov_b32 s4, m0
	s_mov_b32 m0, s28
	s_nop 0
	global_load_lds_dwordx4 v[194:195], off
	s_mov_b32 m0, s4
	v_lshl_add_u64 v[202:203], v[2:3], 0, v[200:201]
	s_add_i32 s26, s29, 0x6000
	s_mov_b32 s4, m0
	s_mov_b32 m0, s26
	s_nop 0
	global_load_lds_dwordx4 v[202:203], off
	s_mov_b32 m0, s4
	v_lshl_add_u64 v[196:197], v[202:203], 0, 64
	s_add_i32 s25, s29, 0x7000
	s_mov_b32 s4, m0
	s_mov_b32 m0, s25
	s_nop 0
	global_load_lds_dwordx4 v[196:197], off
	s_mov_b32 m0, s4
	s_mov_b64 s[4:5], 0x18000
	v_lshl_add_u64 v[2:3], v[198:199], 0, s[4:5]
	s_mov_b64 s[14:15], 0x18040
	v_and_b32_e32 v214, 31, v0
	v_bfe_u32 v215, v0, 5, 1
	s_add_i32 s6, s29, 0x2000
	s_mov_b32 s7, m0
	s_mov_b32 m0, s6
	s_nop 0
	global_load_lds_dwordx4 v[2:3], off
	s_mov_b32 m0, s7
	v_lshl_add_u64 v[2:3], v[198:199], 0, s[14:15]
	s_add_i32 s6, s29, 0x3000
	s_mov_b32 s7, m0
	s_mov_b32 m0, s6
	s_nop 0
	global_load_lds_dwordx4 v[2:3], off
	s_mov_b32 m0, s7
	v_mul_u32_u24_e32 v2, 0x300, v214
	v_lshlrev_b32_e32 v200, 4, v215
	v_lshl_or_b32 v2, v2, 1, v200
	global_load_dwordx4 v[174:177], v2, s[18:19]
	global_load_dwordx4 v[170:173], v2, s[18:19] offset:32
	global_load_dwordx4 v[166:169], v2, s[18:19] offset:64
	global_load_dwordx4 v[162:165], v2, s[18:19] offset:96
	s_mov_b64 s[6:7], 0x30000
	s_mov_b64 s[8:9], 0x30040
	v_lshlrev_b32_e32 v2, 10, v215
	v_lshlrev_b32_e32 v3, 4, v214
	v_add3_u32 v218, 0, v2, v3
	v_lshl_add_u64 v[2:3], v[198:199], 0, s[6:7]
	v_lshl_add_u64 v[4:5], v[198:199], 0, s[8:9]
	s_add_i32 s8, s29, 0x4000
	s_mov_b32 s17, m0
	s_mov_b32 m0, s8
	s_nop 0
	global_load_lds_dwordx4 v[2:3], off
	s_mov_b32 m0, s17
	s_add_i32 s9, s29, 0x5000
	s_mov_b32 s8, m0
	s_mov_b32 m0, s9
	s_nop 0
	global_load_lds_dwordx4 v[4:5], off
	s_mov_b32 m0, s8
	s_waitcnt vmcnt(6) lgkmcnt(0)
	s_barrier
	ds_read_b128 v[2:5], v218
	ds_read_b128 v[6:9], v218 offset:512
	ds_read_b128 v[34:37], v218 offset:2048
	ds_read_b128 v[38:41], v218 offset:2560
	s_mov_b64 s[8:9], 0x48000
	s_mov_b64 s[18:19], 0x48040
	s_mov_b32 s31, -1
	s_movk_i32 s35, 0x2000
	s_movk_i32 s33, 0x4000
	s_mov_b32 s34, 0x41000000
	s_waitcnt vmcnt(3) lgkmcnt(3)
	v_mfma_f32_32x32x16_f16 v[18:33], v[2:5], v[174:177], 0
	s_waitcnt lgkmcnt(2)
	v_mfma_f32_32x32x16_f16 v[2:17], v[6:9], v[174:177], 0
	s_waitcnt vmcnt(2) lgkmcnt(1)
	v_mfma_f32_32x32x16_f16 v[18:33], v[34:37], v[170:173], v[18:33]
	s_waitcnt lgkmcnt(0)
	v_mfma_f32_32x32x16_f16 v[2:17], v[38:41], v[170:173], v[2:17]
	ds_read_b128 v[34:37], v218 offset:4096
	ds_read_b128 v[38:41], v218 offset:4608
	s_waitcnt vmcnt(1) lgkmcnt(1)
	v_mfma_f32_32x32x16_f16 v[18:33], v[34:37], v[166:169], v[18:33]
	s_waitcnt lgkmcnt(0)
	v_mfma_f32_32x32x16_f16 v[2:17], v[38:41], v[166:169], v[2:17]
	ds_read_b128 v[34:37], v218 offset:6144
	ds_read_b128 v[38:41], v218 offset:6656
	s_waitcnt vmcnt(0) lgkmcnt(1)
	v_mfma_f32_32x32x16_f16 v[18:33], v[34:37], v[162:165], v[18:33]
	s_waitcnt lgkmcnt(0)
	v_mfma_f32_32x32x16_f16 v[2:17], v[38:41], v[162:165], v[2:17]
	s_nop 9
	v_max_f32_e32 v34, v19, v19
	v_max_f32_e32 v35, v18, v18
	v_max_f32_e32 v34, v35, v34
	v_max3_f32 v36, v20, v21, v3
	v_max3_f32 v34, v34, v2, v4
	v_max3_f32 v35, v36, v24, v25
	v_max3_f32 v34, v34, v5, v22
	v_max3_f32 v35, v35, v8, v9
	v_max3_f32 v34, v34, v23, v6
	v_max3_f32 v35, v35, v28, v29
	v_max3_f32 v34, v34, v7, v26
	v_max3_f32 v35, v35, v12, v13
	v_max3_f32 v34, v34, v27, v10
	v_max3_f32 v35, v35, v32, v33
	v_max3_f32 v34, v34, v11, v30
	v_max3_f32 v35, v35, v16, v17
	v_max3_f32 v34, v34, v31, v14
	v_max3_f32 v34, v34, v15, v35
	v_mov_b32_e32 v35, v34
	s_nop 1
	v_permlane32_swap_b32_e32 v34, v35
	v_max_f32_e32 v35, v35, v35
	v_max_f32_e32 v34, v34, v34
	v_max_f32_e32 v219, v34, v35
	v_xor_b32_e32 v34, 0x80000000, v219
	v_mov_b32_e32 v35, v34
	v_mov_b32_e32 v36, v34
	v_mov_b32_e32 v37, v34
	v_mov_b32_e32 v38, v34
	v_mov_b32_e32 v39, v34
	v_mov_b32_e32 v40, v34
	v_mov_b32_e32 v41, v34
	v_mov_b32_e32 v42, v34
	v_mov_b32_e32 v43, v34
	v_mov_b32_e32 v44, v34
	v_mov_b32_e32 v45, v34
	v_mov_b32_e32 v46, v34
	v_mov_b32_e32 v47, v34
	v_mov_b32_e32 v48, v34
	v_mov_b32_e32 v49, v34
	s_waitcnt vmcnt(0) lgkmcnt(0)
	s_barrier
	v_sub_f32_e32 v51, v2, v219
	v_sub_f32_e32 v52, v3, v219
	v_lshl_add_u64 v[2:3], v[198:199], 0, s[8:9]
	s_mov_b32 s17, m0
	s_mov_b32 m0, s29
	s_nop 0
	global_load_lds_dwordx4 v[2:3], off
	s_mov_b32 m0, s17
	v_lshl_add_u64 v[2:3], v[198:199], 0, s[18:19]
	s_mov_b32 s17, m0
	s_mov_b32 m0, s28
	s_nop 0
	global_load_lds_dwordx4 v[2:3], off
	s_mov_b32 m0, s17
	s_add_i32 s17, s29, 0x8000
	v_lshl_add_u64 v[2:3], v[202:203], 0, s[4:5]
	s_mov_b32 s4, m0
	s_mov_b32 m0, s17
	s_nop 0
	global_load_lds_dwordx4 v[2:3], off
	s_mov_b32 m0, s4
	s_add_i32 s4, s29, 0x9000
	v_lshl_add_u64 v[2:3], v[202:203], 0, s[14:15]
	s_mov_b32 s5, m0
	s_mov_b32 m0, s4
	s_nop 0
	global_load_lds_dwordx4 v[2:3], off
	s_mov_b32 m0, s5
	ds_read_b128 v[82:85], v218 offset:8192
	ds_read_b128 v[182:185], v218 offset:8704
	ds_read_b128 v[178:181], v218 offset:10240
	ds_read_b128 v[142:145], v218 offset:10752
	ds_read_b128 v[138:141], v218 offset:12288
	ds_read_b128 v[134:137], v218 offset:12800
	ds_read_b128 v[130:133], v218 offset:14336
	ds_read_b128 v[126:129], v218 offset:14848
	v_lshlrev_b32_e32 v2, 1, v0
	v_and_b32_e32 v2, 32, v2
	v_sub_f32_e32 v18, v18, v219
	v_sub_f32_e32 v19, v19, v219
	v_sub_f32_e32 v20, v20, v219
	v_sub_f32_e32 v21, v21, v219
	v_sub_f32_e32 v22, v22, v219
	v_sub_f32_e32 v23, v23, v219
	v_sub_f32_e32 v24, v24, v219
	v_sub_f32_e32 v25, v25, v219
	v_sub_f32_e32 v26, v26, v219
	v_sub_f32_e32 v27, v27, v219
	v_sub_f32_e32 v28, v28, v219
	v_sub_f32_e32 v29, v29, v219
	v_sub_f32_e32 v30, v30, v219
	v_sub_f32_e32 v31, v31, v219
	v_sub_f32_e32 v32, v32, v219
	v_sub_f32_e32 v33, v33, v219
	v_sub_f32_e32 v4, v4, v219
	v_sub_f32_e32 v5, v5, v219
	v_sub_f32_e32 v6, v6, v219
	v_sub_f32_e32 v7, v7, v219
	v_sub_f32_e32 v8, v8, v219
	v_sub_f32_e32 v9, v9, v219
	v_sub_f32_e32 v10, v10, v219
	v_sub_f32_e32 v11, v11, v219
	v_sub_f32_e32 v12, v12, v219
	v_sub_f32_e32 v13, v13, v219
	v_sub_f32_e32 v14, v14, v219
	v_sub_f32_e32 v15, v15, v219
	v_sub_f32_e32 v16, v16, v219
	v_sub_f32_e32 v17, v17, v219
	v_add3_u32 v2, 0, v2, v50
	v_lshlrev_b32_e32 v3, 8, v215
	v_and_b32_e32 v50, 0xc0, v1
	v_add3_u32 v216, v2, v3, v50
	v_exp_f32_e32 v66, v18
	v_exp_f32_e32 v67, v19
	v_exp_f32_e32 v50, v51
	v_exp_f32_e32 v51, v52
	v_exp_f32_e32 v68, v20
	v_exp_f32_e32 v52, v4
	v_exp_f32_e32 v69, v21
	v_exp_f32_e32 v53, v5
	v_exp_f32_e32 v70, v22
	v_exp_f32_e32 v54, v6
	v_exp_f32_e32 v71, v23
	v_exp_f32_e32 v55, v7
	v_exp_f32_e32 v72, v24
	v_exp_f32_e32 v56, v8
	v_exp_f32_e32 v73, v25
	v_exp_f32_e32 v57, v9
	v_exp_f32_e32 v74, v26
	v_exp_f32_e32 v58, v10
	v_exp_f32_e32 v75, v27
	v_exp_f32_e32 v59, v11
	v_exp_f32_e32 v76, v28
	v_exp_f32_e32 v60, v12
	v_exp_f32_e32 v77, v29
	v_exp_f32_e32 v61, v13
	v_exp_f32_e32 v78, v30
	v_exp_f32_e32 v62, v14
	v_exp_f32_e32 v79, v31
	v_exp_f32_e32 v63, v15
	v_exp_f32_e32 v80, v32
	v_exp_f32_e32 v64, v16
	v_exp_f32_e32 v81, v33
	v_exp_f32_e32 v65, v17
	s_lshl_b32 s4, s16, 2
	s_waitcnt vmcnt(4) lgkmcnt(0)
	s_barrier
	s_add_i32 s30, s4, 0
	v_cmp_gt_u32_e64 s[4:5], 32, v212
	s_mov_b64 s[14:15], 0
	s_mov_b64 s[16:17], 0x60000
	s_mov_b64 s[18:19], 0x78000
	v_mov_b32_e32 v2, v201
	v_mov_b32_e32 v3, v201
	v_mov_b32_e32 v4, v201
	v_mov_b32_e32 v5, v201
	v_mov_b32_e32 v6, v201
	v_mov_b32_e32 v7, v201
	v_mov_b32_e32 v8, v201
	v_mov_b32_e32 v9, v201
	v_mov_b32_e32 v10, v201
	v_mov_b32_e32 v11, v201
	v_mov_b32_e32 v12, v201
	v_mov_b32_e32 v13, v201
	v_mov_b32_e32 v14, v201
	v_mov_b32_e32 v15, v201
	v_mov_b32_e32 v16, v201
	v_mov_b32_e32 v17, v201
	v_mov_b32_e32 v18, v201
	v_mov_b32_e32 v19, v201
	v_mov_b32_e32 v20, v201
	v_mov_b32_e32 v21, v201
	v_mov_b32_e32 v22, v201
	v_mov_b32_e32 v23, v201
	v_mov_b32_e32 v24, v201
	v_mov_b32_e32 v25, v201
	v_mov_b32_e32 v26, v201
	v_mov_b32_e32 v27, v201
	v_mov_b32_e32 v28, v201
	v_mov_b32_e32 v29, v201
	v_mov_b32_e32 v30, v201
	v_mov_b32_e32 v31, v201
	v_mov_b32_e32 v32, v201
	v_mov_b32_e32 v33, v201
	v_lshl_add_u32 v217, v214, 2, s30
